# attention segment prologue (both variants): the four first-tile LDS-DMA loads issued together instead of in two groups separated by a full wait
# speedup vs baseline: 1.0032x; 1.0010x over previous
.LBB0_1252:
	s_and_b64 s[18:19], s[16:17], exec
	s_cselect_b32 s29, s26, s27
	s_lshl_b32 s18, s29, 6
	s_add_i32 s18, s18, s28
	v_or_b32_e32 v214, s18, v245
	v_mov_b64_e32 v[0:1], s[2:3]
	v_mad_i64_i32 v[2:3], s[30:31], v214, s96, v[0:1]
	v_lshl_add_u64 v[2:3], v[2:3], 0, s[14:15]
	v_mov_b32_e32 v191, v33
	v_or_b32_e32 v212, 16, v214
	v_lshl_add_u64 v[2:3], v[2:3], 0, v[190:191]
	s_mov_b64 s[34:35], 0x5000
	v_mad_i64_i32 v[0:1], s[30:31], v212, s96, v[0:1]
	v_lshl_add_u64 v[4:5], v[2:3], 0, s[34:35]
	v_add_co_u32_e32 v2, vcc, 0x5000, v2
	v_lshl_add_u64 v[0:1], v[0:1], 0, s[14:15]
	s_nop 0
	v_addc_co_u32_e32 v3, vcc, 0, v3, vcc
	v_lshl_add_u64 v[0:1], v[0:1], 0, v[190:191]
	s_mov_b32 m0, s21
	global_load_dwordx4 v[70:73], v[4:5], off offset:64
	global_load_dwordx4 v[74:77], v[4:5], off offset:128
	global_load_dwordx4 v[78:81], v[2:3], off
	global_load_dwordx4 v[82:85], v[4:5], off offset:192
	v_lshl_add_u64 v[2:3], v[0:1], 0, s[34:35]
	v_add_co_u32_e32 v0, vcc, 0x5000, v0
	s_ashr_i32 s19, s18, 31
	s_nop 0
	v_addc_co_u32_e32 v1, vcc, 0, v1, vcc
	global_load_dwordx4 v[86:89], v[2:3], off offset:64
	global_load_dwordx4 v[90:93], v[2:3], off offset:128
	global_load_dwordx4 v[94:97], v[0:1], off
	global_load_dwordx4 v[98:101], v[2:3], off offset:192
	s_barrier
	global_load_lds_dwordx4 v32, s[0:1]
	s_add_i32 m0, s21, 0x8000
	s_lshl_b64 s[18:19], s[18:19], 9
	global_load_lds_dwordx4 v184, s[0:1]
	s_add_i32 m0, s21, 0x400
	s_nop 0
	global_load_lds_dwordx4 v186, s[0:1]
	s_mov_b32 m0, s22
	s_nop 0
	global_load_lds_dwordx4 v188, s[0:1]
	s_add_u32 s18, s24, s18
	s_addc_u32 s19, s25, s19
	v_lshl_add_u64 v[0:1], s[18:19], 0, v[168:169]
	v_lshl_add_u64 v[2:3], s[18:19], 0, v[174:175]
	global_load_dwordx4 v[24:27], v[0:1], off
	global_load_dwordx4 v[28:31], v[2:3], off
	v_lshl_add_u64 v[0:1], s[18:19], 0, v[176:177]
	v_lshl_add_u64 v[2:3], s[18:19], 0, v[178:179]
	global_load_dwordx4 v[38:41], v[0:1], off
	global_load_dwordx4 v[42:45], v[2:3], off
	s_waitcnt vmcnt(0)
	v_add_u32_e32 v46, 0, v168
	v_add_u32_e32 v46, 0x10000, v46
	s_add_u32 s100, s0, 0x240000
	s_addc_u32 s101, s1, 0
	v_mov_b32_e32 v3, 0
	v_mov_b32_e32 v2, 0
	v_mov_b32_e32 v1, 0
	v_mov_b32_e32 v0, 0
	v_mov_b32_e32 v7, 0
	v_mov_b32_e32 v6, 0
	v_mov_b32_e32 v5, 0
	v_mov_b32_e32 v4, 0
	v_mov_b32_e32 v11, 0
	v_mov_b32_e32 v10, 0
	v_mov_b32_e32 v9, 0
	v_mov_b32_e32 v8, 0
	v_mov_b32_e32 v15, 0
	v_mov_b32_e32 v14, 0
	v_mov_b32_e32 v13, 0
	v_mov_b32_e32 v12, 0
	v_mov_b32_e32 v19, 0
	v_mov_b32_e32 v18, 0
	v_mov_b32_e32 v17, 0
	v_mov_b32_e32 v16, 0
	v_mov_b32_e32 v23, 0
	v_mov_b32_e32 v22, 0
	v_mov_b32_e32 v21, 0
	v_mov_b32_e32 v20, 0
	s_cmp_lt_i32 s29, 0
	v_mov_b32_e32 v49, 0
	v_mov_b32_e32 v48, 0
	v_mov_b32_e32 v47, 0
	v_mov_b32_e32 v53, 0
	v_mov_b32_e32 v52, 0
	v_mov_b32_e32 v51, 0
	v_mov_b32_e32 v50, 0
	v_mov_b32_e32 v57, 0
	v_mov_b32_e32 v56, 0
	v_mov_b32_e32 v55, 0
	v_mov_b32_e32 v54, 0
	v_mov_b32_e32 v61, 0
	v_mov_b32_e32 v60, 0
	v_mov_b32_e32 v59, 0
	v_mov_b32_e32 v58, 0
	v_mov_b32_e32 v65, 0
	ds_write_b128 v46, v[24:27]
	ds_write_b128 v46, v[28:31] offset:8192
	ds_write_b128 v46, v[38:41] offset:16384
	ds_write_b128 v46, v[42:45] offset:24576
	s_waitcnt vmcnt(0)
	v_mov_b32_e32 v27, 0
	v_mov_b32_e32 v26, 0
	v_mov_b32_e32 v25, 0
	v_mov_b32_e32 v24, 0
	v_mov_b32_e32 v31, 0
	v_mov_b32_e32 v30, 0
	v_mov_b32_e32 v29, 0
	v_mov_b32_e32 v28, 0
	v_mov_b32_e32 v41, 0
	v_mov_b32_e32 v40, 0
	v_mov_b32_e32 v39, 0
	v_mov_b32_e32 v38, 0
	v_mov_b32_e32 v45, 0
	v_mov_b32_e32 v44, 0
	v_mov_b32_e32 v43, 0
	v_mov_b32_e32 v42, 0
	v_mov_b32_e32 v46, 0
	v_mov_b32_e32 v64, 0
	v_mov_b32_e32 v63, 0
	v_mov_b32_e32 v62, 0
	v_mov_b32_e32 v69, 0
	v_mov_b32_e32 v68, 0
	v_mov_b32_e32 v67, 0
	v_mov_b32_e32 v66, 0
	v_mov_b32_e32 v102, 0
	v_mov_b32_e32 v103, 0
	s_waitcnt vmcnt(0) lgkmcnt(0)
	s_barrier
	s_cbranch_scc1 .LBB0_1251
	v_mov_b32_e32 v66, v33
	v_mov_b32_e32 v67, v33
	v_mov_b32_e32 v68, v33
	v_mov_b32_e32 v69, v33
	v_mov_b64_e32 v[62:63], v[66:67]
	v_mov_b64_e32 v[58:59], v[66:67]
	v_mov_b64_e32 v[54:55], v[66:67]
	v_mov_b64_e32 v[50:51], v[66:67]
	v_mov_b64_e32 v[46:47], v[66:67]
	v_mov_b64_e32 v[42:43], v[66:67]
	v_mov_b64_e32 v[38:39], v[66:67]
	v_mov_b64_e32 v[28:29], v[66:67]
	v_mov_b64_e32 v[24:25], v[66:67]
	v_mov_b64_e32 v[20:21], v[66:67]
	v_mov_b64_e32 v[16:17], v[66:67]
	v_mov_b64_e32 v[12:13], v[66:67]
	v_mov_b64_e32 v[8:9], v[66:67]
	v_mov_b64_e32 v[4:5], v[66:67]
	v_mov_b64_e32 v[0:1], v[66:67]
	s_add_i32 s30, s29, 1
	s_mov_b32 s31, 0
	v_mov_b32_e32 v218, 0xf149f2ca
	v_mov_b32_e32 v215, 0
	v_mov_b32_e32 v213, v246
	v_mov_b32_e32 v248, 0
	v_mov_b32_e32 v167, 0xf149f2ca
	v_mov_b64_e32 v[64:65], v[68:69]
	v_mov_b64_e32 v[60:61], v[68:69]
	v_mov_b64_e32 v[56:57], v[68:69]
	v_mov_b64_e32 v[52:53], v[68:69]
	v_mov_b64_e32 v[48:49], v[68:69]
	v_mov_b64_e32 v[44:45], v[68:69]
	v_mov_b64_e32 v[40:41], v[68:69]
	v_mov_b64_e32 v[30:31], v[68:69]
	v_mov_b64_e32 v[26:27], v[68:69]
	v_mov_b64_e32 v[22:23], v[68:69]
	v_mov_b64_e32 v[18:19], v[68:69]
	v_mov_b64_e32 v[14:15], v[68:69]
	v_mov_b64_e32 v[10:11], v[68:69]
	v_mov_b64_e32 v[6:7], v[68:69]
	v_mov_b64_e32 v[2:3], v[68:69]
	s_and_b32 s34, s31, 1
	s_cmp_lt_i32 s31, s29
	s_mov_b64 s[18:19], -1
	s_cbranch_scc1 .LBB0_1256
	s_branch .LBB0_1255

.LBB0_1281:
	s_and_b64 s[8:9], s[6:7], exec
	s_cselect_b32 s16, s13, s14
	s_lshl_b32 s8, s16, 6
	s_add_i32 s8, s8, s15
	v_or_b32_e32 v214, s8, v177
	v_mov_b64_e32 v[0:1], s[2:3]
	v_mad_i64_i32 v[2:3], s[18:19], v214, s96, v[0:1]
	v_lshl_add_u64 v[2:3], v[2:3], 0, s[4:5]
	v_mov_b32_e32 v191, v33
	v_or_b32_e32 v212, 16, v214
	v_lshl_add_u64 v[2:3], v[2:3], 0, v[190:191]
	s_mov_b64 s[20:21], 0x5000
	v_mad_i64_i32 v[0:1], s[18:19], v212, s96, v[0:1]
	v_lshl_add_u64 v[4:5], v[2:3], 0, s[20:21]
	v_add_co_u32_e32 v2, vcc, 0x5000, v2
	v_lshl_add_u64 v[0:1], v[0:1], 0, s[4:5]
	s_nop 0
	v_addc_co_u32_e32 v3, vcc, 0, v3, vcc
	v_lshl_add_u64 v[0:1], v[0:1], 0, v[190:191]
	s_mov_b32 m0, s11
	global_load_dwordx4 v[70:73], v[4:5], off offset:64
	global_load_dwordx4 v[74:77], v[4:5], off offset:128
	global_load_dwordx4 v[78:81], v[2:3], off
	global_load_dwordx4 v[82:85], v[4:5], off offset:192
	v_lshl_add_u64 v[2:3], v[0:1], 0, s[20:21]
	v_add_co_u32_e32 v0, vcc, 0x5000, v0
	s_ashr_i32 s9, s8, 31
	s_nop 0
	v_addc_co_u32_e32 v1, vcc, 0, v1, vcc
	global_load_dwordx4 v[86:89], v[2:3], off offset:64
	global_load_dwordx4 v[90:93], v[2:3], off offset:128
	global_load_dwordx4 v[94:97], v[0:1], off
	global_load_dwordx4 v[98:101], v[2:3], off offset:192
	s_barrier
	global_load_lds_dwordx4 v32, s[0:1]
	s_add_i32 m0, s11, 0x8000
	s_lshl_b64 s[8:9], s[8:9], 9
	global_load_lds_dwordx4 v166, s[0:1]
	s_add_i32 m0, s11, 0x400
	s_nop 0
	global_load_lds_dwordx4 v186, s[0:1]
	s_add_i32 m0, s11, 0x8400
	s_nop 0
	global_load_lds_dwordx4 v188, s[0:1]
	s_waitcnt vmcnt(0)
	v_add_u32_e32 v24, 0, v168
	s_add_u32 s100, s0, 0x240000
	s_addc_u32 s101, s1, 0
	s_add_u32 s8, s24, s8
	s_addc_u32 s9, s25, s9
	v_lshl_add_u64 v[0:1], s[8:9], 0, v[168:169]
	v_lshl_add_u64 v[2:3], s[8:9], 0, v[180:181]
	global_load_dwordx4 v[28:31], v[0:1], off
	global_load_dwordx4 v[38:41], v[2:3], off
	v_lshl_add_u64 v[0:1], s[8:9], 0, v[182:183]
	v_lshl_add_u64 v[2:3], s[8:9], 0, v[184:185]
	global_load_dwordx4 v[42:45], v[0:1], off
	global_load_dwordx4 v[46:49], v[2:3], off
	v_add_u32_e32 v24, 0x10000, v24
	v_mov_b32_e32 v3, 0
	v_mov_b32_e32 v2, 0
	v_mov_b32_e32 v1, 0
	v_mov_b32_e32 v0, 0
	v_mov_b32_e32 v7, 0
	v_mov_b32_e32 v6, 0
	v_mov_b32_e32 v5, 0
	v_mov_b32_e32 v4, 0
	v_mov_b32_e32 v11, 0
	v_mov_b32_e32 v10, 0
	v_mov_b32_e32 v9, 0
	v_mov_b32_e32 v8, 0
	v_mov_b32_e32 v15, 0
	v_mov_b32_e32 v14, 0
	v_mov_b32_e32 v13, 0
	v_mov_b32_e32 v12, 0
	v_mov_b32_e32 v19, 0
	v_mov_b32_e32 v18, 0
	v_mov_b32_e32 v17, 0
	v_mov_b32_e32 v16, 0
	v_mov_b32_e32 v23, 0
	v_mov_b32_e32 v22, 0
	v_mov_b32_e32 v21, 0
	v_mov_b32_e32 v20, 0
	v_mov_b32_e32 v27, 0
	s_cmp_lt_i32 s16, 0
	v_mov_b32_e32 v26, 0
	v_mov_b32_e32 v25, 0
	v_mov_b32_e32 v53, 0
	v_mov_b32_e32 v52, 0
	v_mov_b32_e32 v51, 0
	v_mov_b32_e32 v50, 0
	v_mov_b32_e32 v57, 0
	v_mov_b32_e32 v56, 0
	v_mov_b32_e32 v55, 0
	v_mov_b32_e32 v54, 0
	v_mov_b32_e32 v61, 0
	v_mov_b32_e32 v60, 0
	v_mov_b32_e32 v59, 0
	v_mov_b32_e32 v58, 0
	v_mov_b32_e32 v65, 0
	v_mov_b32_e32 v64, 0
	s_waitcnt vmcnt(0)
	ds_write_b128 v24, v[28:31]
	ds_write_b128 v24, v[38:41] offset:8192
	ds_write_b128 v24, v[42:45] offset:16384
	ds_write_b128 v24, v[46:49] offset:24576
	s_waitcnt vmcnt(0)
	v_mov_b32_e32 v24, 0
	v_mov_b32_e32 v31, 0
	v_mov_b32_e32 v30, 0
	v_mov_b32_e32 v29, 0
	v_mov_b32_e32 v28, 0
	v_mov_b32_e32 v45, 0
	v_mov_b32_e32 v44, 0
	v_mov_b32_e32 v43, 0
	v_mov_b32_e32 v42, 0
	v_mov_b32_e32 v41, 0
	v_mov_b32_e32 v40, 0
	v_mov_b32_e32 v39, 0
	v_mov_b32_e32 v38, 0
	v_mov_b32_e32 v49, 0
	v_mov_b32_e32 v48, 0
	v_mov_b32_e32 v47, 0
	v_mov_b32_e32 v46, 0
	v_mov_b32_e32 v63, 0
	v_mov_b32_e32 v62, 0
	v_mov_b32_e32 v69, 0
	v_mov_b32_e32 v68, 0
	v_mov_b32_e32 v67, 0
	v_mov_b32_e32 v66, 0
	v_mov_b32_e32 v102, 0
	v_mov_b32_e32 v103, 0
	s_waitcnt lgkmcnt(0)
	s_barrier
	s_cbranch_scc1 .LBB0_1280
	v_mov_b32_e32 v66, v33
	v_mov_b32_e32 v67, v33
	v_mov_b32_e32 v68, v33
	v_mov_b32_e32 v69, v33
	v_mov_b64_e32 v[62:63], v[66:67]
	v_mov_b64_e32 v[58:59], v[66:67]
	v_mov_b64_e32 v[54:55], v[66:67]
	v_mov_b64_e32 v[50:51], v[66:67]
	v_mov_b64_e32 v[46:47], v[66:67]
	v_mov_b64_e32 v[38:39], v[66:67]
	v_mov_b64_e32 v[42:43], v[66:67]
	v_mov_b64_e32 v[28:29], v[66:67]
	v_mov_b64_e32 v[24:25], v[66:67]
	v_mov_b64_e32 v[20:21], v[66:67]
	v_mov_b64_e32 v[16:17], v[66:67]
	v_mov_b64_e32 v[12:13], v[66:67]
	v_mov_b64_e32 v[8:9], v[66:67]
	v_mov_b64_e32 v[4:5], v[66:67]
	v_mov_b64_e32 v[0:1], v[66:67]
	s_add_i32 s17, s16, 1
	s_mov_b32 s18, 0
	v_mov_b32_e32 v246, 0xf149f2ca
	v_mov_b32_e32 v215, 0
	v_mov_b32_e32 v213, v243
	v_mov_b32_e32 v245, 0
	v_mov_b32_e32 v218, 0xf149f2ca
	v_mov_b64_e32 v[64:65], v[68:69]
	v_mov_b64_e32 v[60:61], v[68:69]
	v_mov_b64_e32 v[56:57], v[68:69]
	v_mov_b64_e32 v[52:53], v[68:69]
	v_mov_b64_e32 v[48:49], v[68:69]
	v_mov_b64_e32 v[40:41], v[68:69]
	v_mov_b64_e32 v[44:45], v[68:69]
	v_mov_b64_e32 v[30:31], v[68:69]
	v_mov_b64_e32 v[26:27], v[68:69]
	v_mov_b64_e32 v[22:23], v[68:69]
	v_mov_b64_e32 v[18:19], v[68:69]
	v_mov_b64_e32 v[14:15], v[68:69]
	v_mov_b64_e32 v[10:11], v[68:69]
	v_mov_b64_e32 v[6:7], v[68:69]
	v_mov_b64_e32 v[2:3], v[68:69]
	s_and_b32 s20, s18, 1
	s_cmp_lt_i32 s18, s16
	s_mov_b64 s[8:9], -1
	s_cbranch_scc1 .LBB0_1285
	s_branch .LBB0_1284
